# bg_take claims all its conversion steps with one atomic instead of one per step (on top of gates epilogue rewrite)
# baseline (speedup 1.0000x reference)
; #define LAS __attribute__((address_space(3)))
; __device__ __forceinline__ unsigned pk2(float lo, float hi) { return f2bf(lo) | (f2bf(hi) << 16); }
; #define PHASE_BEGIN() Ctx c = c0; { int t_ = c0.tid; asm volatile("" : "+v"(t_)); c.tid = t_; c.lane = t_ & 63; c.wave = __builtin_amdgcn_readfirstlane(t_ >> 6); } \
;     GAS unsigned char* wsb = (GAS unsigned char*)a.ws; asm volatile("" : "+s"(wsb));
; __device__ __forceinline__ void tr_item(const float* W, int ldw, int k0, int n0, bf16* WT, int ldt, int drow0, LAS float* scr, int lane, const float* kscale = nullptr) {
;     ...
;     LAS float* wp = scr + (lane >> 4) * 65 + (lane & 15) * 4;
; #pragma unroll
;     for (int i = 0; i < 16; ++i) { LAS float* q = wp + (4 * i) * 65; const float ks = kscale ? kscale[k0 + 4 * i + (lane >> 4)] : 1.f; q[0] = v[i].x * ks; q[1] = v[i].y * ks; q[2] = v[i].z * ks; q[3] = v[i].w * ks; }
;     asm volatile("s_waitcnt lgkmcnt(0)" ::: "memory");
;     const int kc = lane & 7;
; #pragma unroll
;     for (int j = 0; j < 8; ++j) { const int n = (lane >> 3) + 8 * j; const LAS float* sp = scr + (8 * kc) * 65 + n;
;         u32x4 o; o.x = pk2(sp[0 * 65], sp[1 * 65]); o.y = pk2(sp[2 * 65], sp[3 * 65]); o.z = pk2(sp[4 * 65], sp[5 * 65]); o.w = pk2(sp[6 * 65], sp[7 * 65]);
; __device__ __forceinline__ void bg_take(const Args& a, const Ctx& c0, int n) {
;     PHASE_BEGIN();
;     unsigned* head = WSP(unsigned, WS_CTL) + CW_QHEAD;
;     volatile LAS unsigned* bc = (volatile LAS unsigned*)(c.lds + LDS_MISC + 64);
;     LAS float* scr = (LAS float*)(c.lds + c.wave * 16640);
;     __syncthreads();
.LBB0_1254:
	v_mov_b32_e32 v2, v0
	v_readlane_b32 s8, v254, 21
	v_readlane_b32 s10, v254, 23
	v_readfirstlane_b32 s2, v2
	v_readlane_b32 s11, v254, 24
	s_ashr_i32 s15, s2, 6
	s_mov_b64 s[6:7], s[10:11]
	s_waitcnt lgkmcnt(0)
	v_lshlrev_b32_e32 v3, 2, v2
	s_add_u32 s2, s6, 0x8000
	s_mul_i32 s8, s15, 0x4100
	v_bfe_u32 v67, v2, 4, 2
	v_and_b32_e32 v66, 60, v3
	s_addc_u32 s3, s7, 0
	s_add_i32 s8, s8, 0
	v_cmp_eq_u32_e64 s[40:41], 0, v2
	v_mul_u32_u24_e32 v3, 0x104, v67
	v_lshlrev_b32_e32 v4, 2, v66
	v_bfe_u32 v96, v2, 3, 3
	v_lshlrev_b32_e32 v2, 3, v2
	v_add3_u32 v95, s8, v3, v4
	v_and_b32_e32 v2, 56, v2
	v_mov_b32_e32 v3, v147
	v_mul_u32_u24_e32 v6, 0x104, v2
	v_lshl_add_u64 v[4:5], s[6:7], 0, v[2:3]
	v_lshlrev_b32_e32 v3, 2, v96
	v_add3_u32 v97, s8, v6, v3
	v_lshlrev_b32_e32 v2, 1, v2
	v_mov_b32_e32 v3, v147
	v_lshl_add_u64 v[2:3], s[6:7], 0, v[2:3]
	s_mov_b64 s[6:7], 0x1bc00000
	v_lshl_add_u64 v[72:73], v[2:3], 0, s[6:7]
	s_mov_b64 s[6:7], 0x1b800000
	v_lshl_add_u64 v[74:75], v[2:3], 0, s[6:7]
	s_mov_b64 s[6:7], 0x1b600000
	v_lshl_add_u64 v[76:77], v[2:3], 0, s[6:7]
	s_mov_b64 s[6:7], 0x1aa00000
	v_lshl_add_u64 v[78:79], v[2:3], 0, s[6:7]
	s_mov_b64 s[6:7], 0x12a00000
	v_lshl_add_u64 v[80:81], v[4:5], 0, s[6:7]
	s_mov_b64 s[6:7], 0x2a00000
	v_lshl_add_u64 v[82:83], v[4:5], 0, s[6:7]
	s_mov_b64 s[6:7], 0x2200000
	v_lshl_add_u64 v[84:85], v[2:3], 0, s[6:7]
	s_mov_b64 s[6:7], 0x1e00000
	v_readlane_b32 s9, v254, 22
	v_lshl_add_u64 v[86:87], v[2:3], 0, s[6:7]
	s_mov_b64 s[6:7], 0x1c00000
	s_mov_b64 s[10:11], 0x2c400000
	s_mov_b64 s[8:9], 0x1c400000
	v_lshl_add_u64 v[88:89], v[2:3], 0, s[6:7]
	s_mov_b64 s[6:7], 0x1000000
	v_lshl_add_u64 v[68:69], v[4:5], 0, s[10:11]
	v_or_b32_e32 v98, 8, v96
	v_or_b32_e32 v99, 16, v96
	v_or_b32_e32 v100, 24, v96
	v_or_b32_e32 v101, 32, v96
	v_or_b32_e32 v102, 40, v96
	v_or_b32_e32 v103, 48, v96
	v_or_b32_e32 v104, 56, v96
	v_lshl_add_u64 v[70:71], v[4:5], 0, s[8:9]
	v_lshl_add_u64 v[90:91], v[2:3], 0, s[6:7]
	s_waitcnt vmcnt(0)
	s_barrier
	v_writelane_b32 v255, -1, 40
	s_branch .LBB0_1256

; __device__ __forceinline__ void bg_take(const Args& a, const Ctx& c0, int n) {
;     ...
;     for (int i = 0; i < n; ++i) {
;         if (c.tid == 0) { unsigned s = __hip_atomic_fetch_add(head, 1u, __ATOMIC_RELAXED, __HIP_MEMORY_SCOPE_AGENT); if (s >= (unsigned)BG_STEPS) s = 0xffffffffu; bc[0] = s; }
;         __syncthreads();
;         const unsigned s = bc[0];
;         if (s == 0xffffffffu) break;
.LBB0_1256:
	s_and_saveexec_b64 s[6:7], s[40:41]
	s_cbranch_execz .LBB0_1260
	s_mov_b64 s[10:11], exec
	v_mbcnt_lo_u32_b32 v2, s10, 0
	v_mbcnt_hi_u32_b32 v2, s11, v2
	v_cmp_eq_u32_e32 vcc, 0, v2
	s_and_saveexec_b64 s[8:9], vcc
	s_cbranch_execz .LBB0_1259
	v_readlane_b32 s10, v255, 40
	s_nop 3
	s_cmp_lg_u32 s10, -1
	s_cbranch_scc1 .Lbt1_have
	v_mov_b32_e32 v3, s14
	global_atomic_add v3, v147, v3, s[2:3] sc0
	s_waitcnt vmcnt(0)
	v_readfirstlane_b32 s10, v3
	s_nop 3
.Lbt1_have:
	s_add_i32 s11, s10, 1
	v_writelane_b32 v255, s11, 40
	v_mov_b32_e32 v3, s10

; #define LAS __attribute__((address_space(3)))
; __device__ __forceinline__ unsigned pk2(float lo, float hi) { return f2bf(lo) | (f2bf(hi) << 16); }
; #define PHASE_BEGIN() Ctx c = c0; { int t_ = c0.tid; asm volatile("" : "+v"(t_)); c.tid = t_; c.lane = t_ & 63; c.wave = __builtin_amdgcn_readfirstlane(t_ >> 6); } \
;     GAS unsigned char* wsb = (GAS unsigned char*)a.ws; asm volatile("" : "+s"(wsb));
; __device__ __forceinline__ void tr_item(const float* W, int ldw, int k0, int n0, bf16* WT, int ldt, int drow0, LAS float* scr, int lane, const float* kscale = nullptr) {
;     ...
;     LAS float* wp = scr + (lane >> 4) * 65 + (lane & 15) * 4;
; #pragma unroll
;     for (int i = 0; i < 16; ++i) { LAS float* q = wp + (4 * i) * 65; const float ks = kscale ? kscale[k0 + 4 * i + (lane >> 4)] : 1.f; q[0] = v[i].x * ks; q[1] = v[i].y * ks; q[2] = v[i].z * ks; q[3] = v[i].w * ks; }
;     asm volatile("s_waitcnt lgkmcnt(0)" ::: "memory");
;     const int kc = lane & 7;
; #pragma unroll
;     for (int j = 0; j < 8; ++j) { const int n = (lane >> 3) + 8 * j; const LAS float* sp = scr + (8 * kc) * 65 + n;
;         u32x4 o; o.x = pk2(sp[0 * 65], sp[1 * 65]); o.y = pk2(sp[2 * 65], sp[3 * 65]); o.z = pk2(sp[4 * 65], sp[5 * 65]); o.w = pk2(sp[6 * 65], sp[7 * 65]);
; __device__ __forceinline__ void bg_take(const Args& a, const Ctx& c0, int n) {
;     PHASE_BEGIN();
;     unsigned* head = WSP(unsigned, WS_CTL) + CW_QHEAD;
;     volatile LAS unsigned* bc = (volatile LAS unsigned*)(c.lds + LDS_MISC + 64);
;     LAS float* scr = (LAS float*)(c.lds + c.wave * 16640);
;     __syncthreads();
.LBB0_1493:
	v_readlane_b32 s2, v252, 54
	v_readlane_b32 s3, v252, 55
	s_andn2_b64 vcc, exec, s[2:3]
	s_cbranch_vccnz .LBB0_1700
	v_readlane_b32 s2, v254, 54
	v_readlane_b32 s3, v254, 55
	s_and_b64 s[2:3], s[2:3], exec
	v_mov_b32_e32 v1, v0
	v_readlane_b32 s4, v254, 21
	v_readlane_b32 s5, v254, 22
	v_readfirstlane_b32 s2, v1
	v_readlane_b32 s6, v254, 23
	v_readlane_b32 s7, v254, 24
	s_cselect_b32 s10, 26, 24
	s_ashr_i32 s11, s2, 6
	s_mov_b64 s[4:5], s[6:7]
	v_lshlrev_b32_e32 v2, 2, v1
	s_add_u32 s2, s4, 0x8000
	s_mul_i32 s6, s11, 0x4100
	v_bfe_u32 v67, v1, 4, 2
	v_and_b32_e32 v66, 60, v2
	s_addc_u32 s3, s5, 0
	s_add_i32 s6, s6, 0
	v_cmp_eq_u32_e64 s[38:39], 0, v1
	v_mul_u32_u24_e32 v2, 0x104, v67
	s_waitcnt lgkmcnt(0)
	v_lshlrev_b32_e32 v3, 2, v66
	v_bfe_u32 v96, v1, 3, 3
	v_lshlrev_b32_e32 v1, 3, v1
	v_add3_u32 v95, s6, v2, v3
	v_and_b32_e32 v2, 56, v1
	v_mov_b32_e32 v3, v147
	v_mul_u32_u24_e32 v1, 0x104, v2
	v_lshl_add_u64 v[4:5], s[4:5], 0, v[2:3]
	v_lshlrev_b32_e32 v3, 2, v96
	v_add3_u32 v97, s6, v1, v3
	v_lshlrev_b32_e32 v2, 1, v2
	v_mov_b32_e32 v3, v147
	v_lshl_add_u64 v[2:3], s[4:5], 0, v[2:3]
	s_mov_b64 s[4:5], 0x1bc00000
	v_lshl_add_u64 v[72:73], v[2:3], 0, s[4:5]
	s_mov_b64 s[4:5], 0x1b800000
	v_lshl_add_u64 v[74:75], v[2:3], 0, s[4:5]
	s_mov_b64 s[4:5], 0x1b600000
	v_lshl_add_u64 v[76:77], v[2:3], 0, s[4:5]
	s_mov_b64 s[4:5], 0x1aa00000
	v_lshl_add_u64 v[78:79], v[2:3], 0, s[4:5]
	s_mov_b64 s[4:5], 0x12a00000
	v_lshl_add_u64 v[80:81], v[4:5], 0, s[4:5]
	s_mov_b64 s[4:5], 0x2a00000
	v_lshl_add_u64 v[82:83], v[4:5], 0, s[4:5]
	s_mov_b64 s[4:5], 0x2200000
	v_lshl_add_u64 v[84:85], v[2:3], 0, s[4:5]
	s_mov_b64 s[4:5], 0x1e00000
	v_lshl_add_u64 v[86:87], v[2:3], 0, s[4:5]
	s_mov_b64 s[4:5], 0x1c00000
	s_mov_b64 s[8:9], 0x2c400000
	s_mov_b64 s[6:7], 0x1c400000
	v_lshl_add_u64 v[88:89], v[2:3], 0, s[4:5]
	s_mov_b64 s[4:5], 0x1000000
	v_lshl_add_u64 v[68:69], v[4:5], 0, s[8:9]
	v_or_b32_e32 v98, 8, v96
	v_or_b32_e32 v99, 16, v96
	v_or_b32_e32 v100, 24, v96
	v_or_b32_e32 v101, 32, v96
	v_or_b32_e32 v102, 40, v96
	v_or_b32_e32 v103, 48, v96
	v_or_b32_e32 v104, 56, v96
	v_lshl_add_u64 v[70:71], v[4:5], 0, s[6:7]
	v_lshl_add_u64 v[90:91], v[2:3], 0, s[4:5]
	s_waitcnt vmcnt(0)
	s_barrier
	v_writelane_b32 v255, -1, 41
	s_branch .LBB0_1496

; __device__ __forceinline__ void bg_take(const Args& a, const Ctx& c0, int n) {
;     ...
;     for (int i = 0; i < n; ++i) {
;         if (c.tid == 0) { unsigned s = __hip_atomic_fetch_add(head, 1u, __ATOMIC_RELAXED, __HIP_MEMORY_SCOPE_AGENT); if (s >= (unsigned)BG_STEPS) s = 0xffffffffu; bc[0] = s; }
;         __syncthreads();
;         const unsigned s = bc[0];
;         if (s == 0xffffffffu) break;
.LBB0_1496:
	s_and_saveexec_b64 s[4:5], s[38:39]
	s_cbranch_execz .LBB0_1500
	s_mov_b64 s[8:9], exec
	v_mbcnt_lo_u32_b32 v1, s8, 0
	v_mbcnt_hi_u32_b32 v2, s9, v1
	v_cmp_eq_u32_e32 vcc, 0, v2
	s_and_saveexec_b64 s[6:7], vcc
	s_cbranch_execz .LBB0_1499
	v_readlane_b32 s8, v255, 41
	s_nop 3
	s_cmp_lg_u32 s8, -1
	s_cbranch_scc1 .Lbt2_have
	v_mov_b32_e32 v1, s10
	global_atomic_add v3, v147, v1, s[2:3] sc0
	s_waitcnt vmcnt(0)
	v_readfirstlane_b32 s8, v3
	s_nop 3
.Lbt2_have:
	s_add_i32 s9, s8, 1
	v_writelane_b32 v255, s9, 41
	v_mov_b32_e32 v3, s8
